# router phase: batch the 8 row loads of the sum-of-squares loop (was 6 serialized round trips)
# baseline (speedup 1.0000x reference)
.LBB6_1829:
	v_ashrrev_i32_e32 v13, 31, v12
	v_readlane_b32 s0, v254, 4
	v_lshlrev_b64 v[4:5], 13, v[12:13]
	v_readlane_b32 s1, v254, 5
	v_readlane_b32 s6, v254, 33
	v_readlane_b32 s7, v254, 34
	v_lshl_add_u64 v[4:5], s[0:1], 0, v[4:5]
	v_lshl_add_u64 v[8:9], v[4:5], 0, v[2:3]
	global_load_dwordx4 v[46:49], v[8:9], off
	global_load_dwordx4 v[50:53], v[8:9], off offset:1024
	global_load_dwordx4 v[54:57], v[8:9], off offset:2048
	global_load_dwordx4 v[58:61], v[8:9], off offset:3072
	v_add_co_u32_e32 v26, vcc, s45, v8
	s_mov_b64 s[8:9], 0
	s_nop 0
	v_addc_co_u32_e32 v27, vcc, 0, v9, vcc
	global_load_dwordx4 v[62:65], v[26:27], off
	global_load_dwordx4 v[66:69], v[26:27], off offset:1024
	global_load_dwordx4 v[70:73], v[26:27], off offset:2048
	global_load_dwordx4 v[74:77], v[26:27], off offset:3072
	s_waitcnt vmcnt(7)
	v_mul_f32_e32 v10, v47, v47
	v_fmac_f32_e32 v10, v46, v46
	v_fmac_f32_e32 v10, v48, v48
	v_fmac_f32_e32 v10, v49, v49
	s_waitcnt vmcnt(6)
	v_mul_f32_e32 v5, v51, v51
	v_fmac_f32_e32 v5, v50, v50
	v_fmac_f32_e32 v5, v52, v52
	v_fmac_f32_e32 v5, v53, v53
	v_add_f32_e32 v10, v10, v5
	s_waitcnt vmcnt(5)
	v_mul_f32_e32 v5, v55, v55
	v_fmac_f32_e32 v5, v54, v54
	v_fmac_f32_e32 v5, v56, v56
	v_fmac_f32_e32 v5, v57, v57
	v_add_f32_e32 v10, v10, v5
	s_waitcnt vmcnt(4)
	v_mul_f32_e32 v5, v59, v59
	v_fmac_f32_e32 v5, v58, v58
	v_fmac_f32_e32 v5, v60, v60
	v_fmac_f32_e32 v5, v61, v61
	v_add_f32_e32 v30, v10, v5
	s_waitcnt vmcnt(2)
	v_mov_b32_e32 v32, v63
	v_mov_b32_e32 v33, v67
	v_pk_mul_f32 v[4:5], v[32:33], v[32:33]
	v_mov_b32_e32 v32, v62
	v_mov_b32_e32 v33, v66
	v_pk_fma_f32 v[4:5], v[32:33], v[32:33], v[4:5]
	v_mov_b32_e32 v32, v64
	v_mov_b32_e32 v33, v68
	v_pk_fma_f32 v[4:5], v[32:33], v[32:33], v[4:5]
	v_mov_b32_e32 v32, v65
	v_mov_b32_e32 v33, v69
	v_pk_fma_f32 v[4:5], v[32:33], v[32:33], v[4:5]
	s_nop 0
	v_add_f32_e32 v4, v30, v4
	v_add_f32_e32 v28, v4, v5
	s_waitcnt vmcnt(0)
	v_mov_b32_e32 v32, v71
	v_mov_b32_e32 v33, v75
	v_pk_mul_f32 v[4:5], v[32:33], v[32:33]
	v_mov_b32_e32 v32, v70
	v_mov_b32_e32 v33, v74
	v_pk_fma_f32 v[4:5], v[32:33], v[32:33], v[4:5]
	v_mov_b32_e32 v32, v72
	v_mov_b32_e32 v33, v76
	v_pk_fma_f32 v[4:5], v[32:33], v[32:33], v[4:5]
	v_mov_b32_e32 v32, v73
	v_mov_b32_e32 v33, v77
	v_pk_fma_f32 v[4:5], v[32:33], v[32:33], v[4:5]
	s_nop 0
	v_add_f32_e32 v4, v28, v4
	v_add_f32_e32 v4, v4, v5
	ds_bpermute_b32 v5, v25, v4
	v_mov_b64_e32 v[28:29], v[20:21]
	s_waitcnt lgkmcnt(0)
	v_add_f32_e32 v4, v4, v5
	ds_bpermute_b32 v5, v40, v4
	s_waitcnt lgkmcnt(0)
	v_add_f32_e32 v4, v4, v5
	ds_bpermute_b32 v5, v41, v4
	s_waitcnt lgkmcnt(0)
	v_add_f32_e32 v4, v4, v5
	ds_bpermute_b32 v5, v42, v4
	s_waitcnt lgkmcnt(0)
	v_add_f32_e32 v4, v4, v5
	ds_bpermute_b32 v5, v43, v4
	s_waitcnt lgkmcnt(0)
	v_add_f32_e32 v4, v4, v5
	ds_bpermute_b32 v5, v44, v4
	s_waitcnt lgkmcnt(0)
	v_add_f32_e32 v4, v4, v5
	v_fmamk_f32 v4, v4, 0x3a000000, v212
	v_cmp_gt_f32_e32 vcc, s58, v4
	v_mul_f32_e32 v5, 0x4b800000, v4
	s_nop 0
	v_cndmask_b32_e32 v4, v4, v5, vcc
	v_rsq_f32_e32 v4, v4
	s_nop 0
	v_mul_f32_e32 v5, 0x45800000, v4
	v_cndmask_b32_e32 v26, v4, v5, vcc
	v_mov_b32_e32 v4, 0
	v_mov_b32_e32 v27, v26
	v_mov_b32_e32 v5, v4
	v_mov_b32_e32 v10, v4
	v_mov_b32_e32 v11, v4
	v_mov_b32_e32 v8, v4
	v_mov_b32_e32 v9, v4
	v_mov_b32_e32 v6, v4
	v_mov_b32_e32 v7, v4
